# router logits loop: x-fragment waits no longer drain the just-issued weight loads of the next chunk (counted waits +6 on the prefetch path)
# baseline (speedup 1.0000x reference)
.Lrouter_a:
	s_waitcnt vmcnt(12)
	v_and_b32_e32 v65, 0xffff0000, v71
	v_and_b32_e32 v64, 0xffff0000, v70
	v_lshlrev_b32_e32 v63, 16, v71
	v_lshlrev_b32_e32 v62, 16, v70
	v_pk_mul_f32 v[112:113], v[64:65], v[64:65]
	v_and_b32_e32 v155, 0xffff0000, v73
	v_and_b32_e32 v154, 0xffff0000, v72
	v_pk_fma_f32 v[112:113], v[62:63], v[62:63], v[112:113]
	v_lshlrev_b32_e32 v153, 16, v73
	v_lshlrev_b32_e32 v152, 16, v72
	v_pk_mul_f32 v[114:115], v[154:155], v[154:155]
	s_waitcnt lgkmcnt(0)
	s_barrier
	v_pk_fma_f32 v[114:115], v[152:153], v[152:153], v[114:115]
	v_add_f32_e32 v74, v112, v113
	ds_read_b128 v[144:147], v125 offset:26112
	ds_read_b128 v[148:151], v125 offset:26128
	v_add_f32_e32 v74, v114, v74
	v_lshlrev_b32_e32 v160, 16, v68
	v_pk_add_f32 v[112:113], v[114:115], v[74:75] op_sel_hi:[1,0]
	v_and_b32_e32 v161, 0xffff0000, v68
	v_mul_f32_e32 v74, v160, v160
	v_mul_f32_e32 v62, 4.0, v62
	v_mul_f32_e32 v64, 4.0, v64
	v_pk_fma_f32 v[116:117], v[160:161], v[160:161], v[74:75] op_sel_hi:[1,1,0]
	v_med3_f32 v74, v62, s50, v140
	v_med3_f32 v64, v64, s50, v140
	v_mov_b32_e32 v62, 0
	v_cvt_pk_fp8_f32 v62, v74, v64
	v_mul_f32_e32 v63, 4.0, v63
	v_mul_f32_e32 v65, 4.0, v65
	v_med3_f32 v63, v63, s50, v140
	v_med3_f32 v64, v65, s50, v140
	v_cvt_pk_fp8_f32 v62, v63, v64 op_sel:[0,0,1]
	v_mul_f32_e32 v63, 4.0, v152
	v_mul_f32_e32 v64, 4.0, v154
	v_mul_f32_e32 v65, 4.0, v153
	v_mul_f32_e32 v74, 4.0, v155
	ds_read_b128 v[152:155], v125 offset:51456
	s_waitcnt lgkmcnt(2)
	v_mfma_f32_16x16x32_bf16 v[58:61], v[144:147], v[70:73], v[58:61]
	ds_read_b128 v[144:147], v125 offset:51472
	v_med3_f32 v110, v63, s50, v140
	v_med3_f32 v64, v64, s50, v140
	s_waitcnt lgkmcnt(2)
	v_mfma_f32_16x16x32_bf16 v[58:61], v[148:151], v[66:69], v[58:61]
	ds_read_b128 v[148:151], v125 offset:34560
	v_mov_b32_e32 v63, 0
	v_cvt_pk_fp8_f32 v63, v110, v64
	s_waitcnt lgkmcnt(2)
	v_mfma_f32_16x16x32_bf16 v[58:61], v[152:155], v[70:73], v[58:61]
	ds_read_b128 v[152:155], v125 offset:34576
	v_lshlrev_b32_e32 v156, 16, v66
	v_and_b32_e32 v158, 0xffff0000, v66
	s_waitcnt lgkmcnt(2)
	v_mfma_f32_16x16x32_bf16 v[58:61], v[144:147], v[66:69], v[58:61]
	ds_read_b128 v[144:147], v125 offset:59904
	v_med3_f32 v65, v65, s50, v140
	v_med3_f32 v64, v74, s50, v140
	s_waitcnt lgkmcnt(2)
	v_mfma_f32_16x16x32_bf16 v[50:53], v[148:151], v[70:73], v[50:53]
	ds_read_b128 v[148:151], v125 offset:59920
	v_cvt_pk_fp8_f32 v63, v65, v64 op_sel:[0,0,1]
	v_mul_f32_e32 v64, 4.0, v156
	s_waitcnt lgkmcnt(2)
	v_mfma_f32_16x16x32_bf16 v[50:53], v[152:155], v[66:69], v[50:53]
	ds_read_b128 v[152:155], v125 offset:43008
	v_mul_f32_e32 v65, 4.0, v158
	v_med3_f32 v112, v64, s50, v140
	s_waitcnt lgkmcnt(2)
	v_mfma_f32_16x16x32_bf16 v[50:53], v[144:147], v[70:73], v[50:53]
	ds_read_b128 v[144:147], v125 offset:43024
	v_med3_f32 v65, v65, s50, v140
	v_mov_b32_e32 v64, 0
	s_waitcnt lgkmcnt(2)
	v_mfma_f32_16x16x32_bf16 v[50:53], v[148:151], v[66:69], v[50:53]
	ds_read_b128 v[148:151], v126 offset:25344
	v_cvt_pk_fp8_f32 v64, v112, v65
	v_lshlrev_b32_e32 v157, 16, v67
	s_waitcnt lgkmcnt(2)
	v_mfma_f32_16x16x32_bf16 v[54:57], v[152:155], v[70:73], v[54:57]
	ds_read_b128 v[152:155], v126 offset:25360
	v_and_b32_e32 v159, 0xffff0000, v67
	v_mul_f32_e32 v74, 4.0, v157
	s_waitcnt lgkmcnt(2)
	v_mfma_f32_16x16x32_bf16 v[54:57], v[144:147], v[66:69], v[54:57]
	v_mul_f32_e32 v110, 4.0, v159
	v_med3_f32 v74, v74, s50, v140
	v_med3_f32 v65, v110, s50, v140
	s_waitcnt lgkmcnt(1)
	v_mfma_f32_16x16x32_bf16 v[54:57], v[148:151], v[70:73], v[54:57]
	v_cvt_pk_fp8_f32 v64, v74, v65 op_sel:[0,0,1]
	v_mul_f32_e32 v65, 4.0, v160
	v_mul_f32_e32 v74, 4.0, v161
	v_med3_f32 v110, v65, s50, v140
	v_med3_f32 v70, v74, s50, v140
	v_mov_b32_e32 v65, 0
	s_waitcnt lgkmcnt(0)
	v_mfma_f32_16x16x32_bf16 v[54:57], v[152:155], v[66:69], v[54:57]
	s_waitcnt vmcnt(10)
	v_and_b32_e32 v149, 0xffff0000, v46
	v_and_b32_e32 v148, 0xffff0000, v48
	v_and_b32_e32 v67, 0xffff0000, v47
	v_cvt_pk_fp8_f32 v65, v110, v70
	v_lshlrev_b32_e32 v73, 16, v46
	v_lshlrev_b32_e32 v72, 16, v48
	v_lshlrev_b32_e32 v66, 16, v47
	v_mul_f32_e32 v68, v67, v67
	v_pk_mul_f32 v[70:71], v[148:149], v[148:149]
	v_lshlrev_b32_e32 v119, 16, v69
	v_and_b32_e32 v121, 0xffff0000, v69
	v_pk_fma_f32 v[68:69], v[66:67], v[66:67], v[68:69] op_sel_hi:[1,1,0]
	v_pk_fma_f32 v[70:71], v[72:73], v[72:73], v[70:71]
	v_lshlrev_b32_e32 v154, 16, v49
	v_pk_add_f32 v[68:69], v[70:71], v[68:69] op_sel:[1,0] op_sel_hi:[0,1]
	v_pk_mul_f32 v[114:115], v[158:159], v[158:159]
	v_pk_add_f32 v[152:153], v[70:71], v[68:69]
	v_and_b32_e32 v155, 0xffff0000, v49
	v_mul_f32_e32 v68, v154, v154
	v_pk_fma_f32 v[114:115], v[156:157], v[156:157], v[114:115]
	v_pk_fma_f32 v[156:157], v[154:155], v[154:155], v[68:69] op_sel_hi:[1,1,0]
	v_mul_f32_e32 v68, 4.0, v73
	v_mul_f32_e32 v69, 4.0, v149
	v_mul_f32_e32 v73, 4.0, v66
	v_med3_f32 v68, v68, s50, v140
	v_med3_f32 v69, v69, s50, v140
	v_mov_b32_e32 v66, 0
	v_cvt_pk_fp8_f32 v66, v68, v69
	ds_read_b128 v[68:71], v125 offset:26240
	ds_read_b128 v[144:147], v125 offset:26256
	v_mul_f32_e32 v67, 4.0, v67
	v_med3_f32 v73, v73, s50, v140
	v_med3_f32 v67, v67, s50, v140
	v_cvt_pk_fp8_f32 v66, v73, v67 op_sel:[0,0,1]
	v_mul_f32_e32 v67, 4.0, v72
	v_mul_f32_e32 v72, 4.0, v148
	ds_read_b128 v[148:151], v125 offset:51584
	s_waitcnt lgkmcnt(2)
	v_mfma_f32_16x16x32_bf16 v[58:61], v[68:71], v[46:49], v[58:61]
	ds_read_b128 v[68:71], v125 offset:51600
	v_mul_f32_e32 v73, 4.0, v154
	v_mul_f32_e32 v154, 4.0, v155
	s_waitcnt lgkmcnt(2)
	v_mfma_f32_16x16x32_bf16 v[58:61], v[144:147], v[42:45], v[58:61]
	ds_read_b128 v[144:147], v125 offset:34688
	v_med3_f32 v155, v67, s50, v140
	v_med3_f32 v72, v72, s50, v140
	s_waitcnt lgkmcnt(2)
	v_mfma_f32_16x16x32_bf16 v[58:61], v[148:151], v[46:49], v[58:61]
	v_mov_b32_e32 v67, 0
	v_cvt_pk_fp8_f32 v67, v155, v72
	ds_read_b128 v[148:151], v125 offset:34704
	v_med3_f32 v73, v73, s50, v140
	s_waitcnt lgkmcnt(2)
	v_mfma_f32_16x16x32_bf16 v[58:61], v[68:71], v[42:45], v[58:61]
	v_med3_f32 v68, v154, s50, v140
	v_cvt_pk_fp8_f32 v67, v73, v68 op_sel:[0,0,1]
	ds_read_b128 v[68:71], v125 offset:60032
	s_waitcnt lgkmcnt(2)
	v_mfma_f32_16x16x32_bf16 v[50:53], v[144:147], v[46:49], v[50:53]
	ds_read_b128 v[144:147], v125 offset:60048
	v_lshlrev_b32_e32 v74, 16, v43
	v_and_b32_e32 v143, 0xffff0000, v43
	s_waitcnt lgkmcnt(2)
	v_mfma_f32_16x16x32_bf16 v[50:53], v[148:151], v[42:45], v[50:53]
	ds_read_b128 v[148:151], v125 offset:43136
	v_pk_add_f32 v[114:115], v[114:115], v[114:115] op_sel_hi:[0,1]
	v_lshlrev_b32_e32 v153, 16, v44
	s_waitcnt lgkmcnt(2)
	v_mfma_f32_16x16x32_bf16 v[50:53], v[68:71], v[46:49], v[50:53]
	ds_read_b128 v[68:71], v125 offset:43152
	v_and_b32_e32 v159, 0xffff0000, v44
	v_mul_f32_e32 v72, 4.0, v74
	s_waitcnt lgkmcnt(1)
	v_mfma_f32_16x16x32_bf16 v[54:57], v[148:151], v[46:49], v[54:57]
	v_mul_f32_e32 v73, 4.0, v143
	v_mul_f32_e32 v116, v74, v74
	v_mul_f32_e32 v114, v143, v143
	v_mfma_f32_16x16x32_bf16 v[50:53], v[144:147], v[42:45], v[50:53]
	ds_read_b128 v[144:147], v127 offset:25344
	v_med3_f32 v74, v72, s50, v140
	v_med3_f32 v143, v73, s50, v140
	v_mul_f32_e32 v72, 4.0, v153
	v_mul_f32_e32 v73, 4.0, v159
	v_med3_f32 v72, v72, s50, v140
	v_med3_f32 v73, v73, s50, v140
	s_waitcnt lgkmcnt(1)
	v_mfma_f32_16x16x32_bf16 v[54:57], v[68:71], v[42:45], v[54:57]
	v_mov_b32_e32 v69, 0
	v_cvt_pk_fp8_f32 v69, v72, v73
	ds_read_b128 v[70:73], v127 offset:25360
	s_waitcnt lgkmcnt(1)
	v_mfma_f32_16x16x32_bf16 v[46:49], v[144:147], v[46:49], v[54:57]
	v_lshlrev_b32_e32 v160, 16, v45
	v_and_b32_e32 v161, 0xffff0000, v45
	v_mul_f32_e32 v110, v153, v153
	v_mul_f32_e32 v54, 4.0, v119
	v_mul_f32_e32 v55, 4.0, v121
	v_mul_f32_e32 v153, 4.0, v160
	v_mul_f32_e32 v154, 4.0, v161
	v_med3_f32 v54, v54, s50, v140
	v_med3_f32 v55, v55, s50, v140
	v_lshlrev_b32_e32 v118, 16, v42
	v_and_b32_e32 v120, 0xffff0000, v42
	v_med3_f32 v148, v153, s50, v140
	v_cvt_pk_fp8_f32 v65, v54, v55 op_sel:[0,0,1]
	v_med3_f32 v54, v154, s50, v140
	v_cvt_pk_fp8_f32 v69, v148, v54 op_sel:[0,0,1]
	s_waitcnt lgkmcnt(0)
	v_mfma_f32_16x16x32_bf16 v[54:57], v[70:73], v[42:45], v[46:49]
	v_mul_f32_e32 v44, 4.0, v118
	v_mul_f32_e32 v45, 4.0, v120
	v_med3_f32 v44, v44, s50, v140
	v_med3_f32 v45, v45, s50, v140
	v_mov_b32_e32 v68, 0
	v_cvt_pk_fp8_f32 v68, v44, v45
	v_pk_mul_f32 v[42:43], v[120:121], v[120:121]
	v_mul_f32_e32 v112, v159, v159
	v_pk_fma_f32 v[42:43], v[118:119], v[118:119], v[42:43]
	v_cvt_pk_fp8_f32 v68, v74, v143 op_sel:[0,0,1]
	v_pk_add_f32 v[44:45], v[116:117], v[114:115]
	v_mul_f32_e32 v156, v160, v160
	v_mul_f32_e32 v158, v161, v161
	v_pk_add_f32 v[42:43], v[42:43], v[44:45]
	v_pk_add_f32 v[44:45], v[110:111], v[112:113]
	v_mov_b32_e32 v159, v152
	v_pk_add_f32 v[42:43], v[42:43], v[44:45]
	v_pk_add_f32 v[44:45], v[156:157], v[158:159]
	global_store_dwordx4 v[106:107], v[66:69], off offset:-64
	v_pk_add_f32 v[42:43], v[42:43], v[44:45]
	s_waitcnt vmcnt(9)
	v_and_b32_e32 v115, 0xffff0000, v41
	v_and_b32_e32 v69, 0xffff0000, v39
	v_and_b32_e32 v68, 0xffff0000, v38
	v_lshlrev_b32_e32 v67, 16, v39
	v_lshlrev_b32_e32 v66, 16, v38
	v_pk_mul_f32 v[44:45], v[68:69], v[68:69]
	v_and_b32_e32 v114, 0xffff0000, v40
	v_pk_add_f32 v[42:43], v[42:43], v[42:43] op_sel_hi:[0,1]
	v_pk_fma_f32 v[44:45], v[66:67], v[66:67], v[44:45]
	v_lshlrev_b32_e32 v73, 16, v41
	v_lshlrev_b32_e32 v72, 16, v40
	v_pk_mul_f32 v[46:47], v[114:115], v[114:115]
	v_add_f32_e32 v42, v44, v45
	v_pk_fma_f32 v[46:47], v[72:73], v[72:73], v[46:47]
	v_lshlrev_b32_e32 v144, 16, v36
	v_add_f32_e32 v42, v46, v42
	v_pk_add_f32 v[44:45], v[46:47], v[42:43] op_sel_hi:[1,0]
	v_and_b32_e32 v145, 0xffff0000, v36
	v_mul_f32_e32 v42, v144, v144
	v_pk_fma_f32 v[48:49], v[144:145], v[144:145], v[42:43] op_sel_hi:[1,1,0]
	v_mul_f32_e32 v44, 4.0, v68
	v_mul_f32_e32 v48, 4.0, v69
	ds_read_b128 v[68:71], v125 offset:26368
	ds_read_b128 v[110:113], v125 offset:26384
	v_and_b32_e32 v121, 0xffff0000, v35
	v_and_b32_e32 v120, 0xffff0000, v34
	v_mul_f32_e32 v42, 4.0, v66
	v_lshlrev_b32_e32 v119, 16, v35
	v_lshlrev_b32_e32 v118, 16, v34
	v_pk_mul_f32 v[46:47], v[120:121], v[120:121]
	v_med3_f32 v42, v42, s50, v140
	v_med3_f32 v44, v44, s50, v140
	v_mov_b32_e32 v66, 0
	v_pk_fma_f32 v[46:47], v[118:119], v[118:119], v[46:47]
	v_cvt_pk_fp8_f32 v66, v42, v44
	v_pk_add_f32 v[46:47], v[46:47], v[46:47] op_sel_hi:[0,1]
	v_mul_f32_e32 v46, 4.0, v67
	v_med3_f32 v42, v46, s50, v140
	v_med3_f32 v44, v48, s50, v140
	v_cvt_pk_fp8_f32 v66, v42, v44 op_sel:[0,0,1]
	v_mul_f32_e32 v44, 4.0, v114
	v_mul_f32_e32 v48, 4.0, v115
	ds_read_b128 v[114:117], v125 offset:51712
	s_waitcnt lgkmcnt(2)
	v_mfma_f32_16x16x32_bf16 v[58:61], v[68:71], v[38:41], v[58:61]
	ds_read_b128 v[68:71], v125 offset:51728
	v_mul_f32_e32 v42, 4.0, v72
	v_mul_f32_e32 v46, 4.0, v73
	s_waitcnt lgkmcnt(2)
	v_mfma_f32_16x16x32_bf16 v[58:61], v[110:113], v[34:37], v[58:61]
	ds_read_b128 v[110:113], v125 offset:34816
	v_med3_f32 v42, v42, s50, v140
	v_med3_f32 v44, v44, s50, v140
	s_waitcnt lgkmcnt(2)
	v_mfma_f32_16x16x32_bf16 v[58:61], v[114:117], v[38:41], v[58:61]
	ds_read_b128 v[114:117], v125 offset:34832
	v_mov_b32_e32 v67, 0
	v_cvt_pk_fp8_f32 v67, v42, v44
	s_waitcnt lgkmcnt(2)
	v_mfma_f32_16x16x32_bf16 v[58:61], v[68:71], v[34:37], v[58:61]
	ds_read_b128 v[68:71], v125 offset:60160
	v_med3_f32 v46, v46, s50, v140
	v_med3_f32 v42, v48, s50, v140
	s_waitcnt lgkmcnt(2)
	v_mfma_f32_16x16x32_bf16 v[50:53], v[110:113], v[38:41], v[50:53]
	ds_read_b128 v[110:113], v125 offset:60176
	v_cvt_pk_fp8_f32 v67, v46, v42 op_sel:[0,0,1]
	v_mul_f32_e32 v42, 4.0, v118
	s_waitcnt lgkmcnt(2)
	v_mfma_f32_16x16x32_bf16 v[50:53], v[114:117], v[34:37], v[50:53]
	ds_read_b128 v[114:117], v125 offset:43264
	v_mul_f32_e32 v44, 4.0, v120
	v_med3_f32 v42, v42, s50, v140
	s_waitcnt lgkmcnt(2)
	v_mfma_f32_16x16x32_bf16 v[50:53], v[68:71], v[38:41], v[50:53]
	ds_read_b128 v[70:73], v125 offset:43280
	v_med3_f32 v44, v44, s50, v140
	v_mov_b32_e32 v68, 0
	s_waitcnt lgkmcnt(2)
	v_mfma_f32_16x16x32_bf16 v[50:53], v[110:113], v[34:37], v[50:53]
	ds_read_b128 v[110:113], v128 offset:25344
	v_cvt_pk_fp8_f32 v68, v42, v44
	v_mul_f32_e32 v46, 4.0, v119
	s_waitcnt lgkmcnt(2)
	v_mfma_f32_16x16x32_bf16 v[54:57], v[114:117], v[38:41], v[54:57]
	ds_read_b128 v[114:117], v128 offset:25360
	v_mul_f32_e32 v48, 4.0, v121
	v_med3_f32 v46, v46, s50, v140
	s_waitcnt lgkmcnt(2)
	v_mfma_f32_16x16x32_bf16 v[54:57], v[70:73], v[34:37], v[54:57]
	v_med3_f32 v42, v48, s50, v140
	v_cvt_pk_fp8_f32 v68, v46, v42 op_sel:[0,0,1]
	v_mul_f32_e32 v42, 4.0, v144
	s_waitcnt lgkmcnt(1)
	v_mfma_f32_16x16x32_bf16 v[38:41], v[110:113], v[38:41], v[54:57]
	v_mul_f32_e32 v44, 4.0, v145
	global_store_dwordx4 v[106:107], v[62:65], off offset:-128
	v_med3_f32 v42, v42, s50, v140
	v_med3_f32 v44, v44, s50, v140
	v_lshlrev_b32_e32 v63, 16, v37
	v_and_b32_e32 v65, 0xffff0000, v37
	v_mov_b32_e32 v69, 0
	s_waitcnt lgkmcnt(0)
	v_mfma_f32_16x16x32_bf16 v[34:37], v[114:117], v[34:37], v[38:41]
	s_waitcnt vmcnt(8)
	v_and_b32_e32 v111, 0xffff0000, v30
	v_and_b32_e32 v110, 0xffff0000, v32
	v_cvt_pk_fp8_f32 v69, v42, v44
	v_and_b32_e32 v39, 0xffff0000, v31
	v_lshlrev_b32_e32 v41, 16, v30
	v_lshlrev_b32_e32 v40, 16, v32
	v_lshlrev_b32_e32 v38, 16, v31
	v_mul_f32_e32 v42, v39, v39
	v_pk_mul_f32 v[56:57], v[110:111], v[110:111]
	v_pk_fma_f32 v[54:55], v[38:39], v[38:39], v[42:43] op_sel_hi:[1,1,0]
	v_pk_fma_f32 v[56:57], v[40:41], v[40:41], v[56:57]
	v_mul_f32_e32 v41, 4.0, v41
	v_pk_add_f32 v[54:55], v[56:57], v[54:55] op_sel:[1,0] op_sel_hi:[0,1]
	v_pk_add_f32 v[114:115], v[56:57], v[54:55]
	v_mul_f32_e32 v54, 4.0, v111
	v_mul_f32_e32 v70, 4.0, v38
	v_med3_f32 v41, v41, s50, v140
	v_med3_f32 v54, v54, s50, v140
	v_mov_b32_e32 v38, 0
	v_cvt_pk_fp8_f32 v38, v41, v54
	ds_read_b128 v[54:57], v125 offset:26496
	v_med3_f32 v41, v70, s50, v140
	ds_read_b128 v[70:73], v125 offset:26512
	v_mul_f32_e32 v39, 4.0, v39
	v_med3_f32 v39, v39, s50, v140
	v_cvt_pk_fp8_f32 v38, v41, v39 op_sel:[0,0,1]
	v_mul_f32_e32 v39, 4.0, v40
	v_mul_f32_e32 v40, 4.0, v110
	ds_read_b128 v[110:113], v125 offset:51840
	s_waitcnt lgkmcnt(2)
	v_mfma_f32_16x16x32_bf16 v[54:57], v[54:57], v[30:33], v[58:61]
	v_lshlrev_b32_e32 v116, 16, v33
	v_and_b32_e32 v117, 0xffff0000, v33
	v_mul_f32_e32 v42, v116, v116
	ds_read_b128 v[58:61], v125 offset:51856
	s_waitcnt lgkmcnt(2)
	v_mfma_f32_16x16x32_bf16 v[54:57], v[70:73], v[26:29], v[54:57]
	ds_read_b128 v[70:73], v125 offset:34944
	v_pk_fma_f32 v[118:119], v[116:117], v[116:117], v[42:43] op_sel_hi:[1,1,0]
	v_mul_f32_e32 v41, 4.0, v116
	s_waitcnt lgkmcnt(2)
	v_mfma_f32_16x16x32_bf16 v[54:57], v[110:113], v[30:33], v[54:57]
	ds_read_b128 v[110:113], v125 offset:34960
	v_mul_f32_e32 v116, 4.0, v117
	v_med3_f32 v117, v39, s50, v140
	s_waitcnt lgkmcnt(2)
	v_mfma_f32_16x16x32_bf16 v[58:61], v[58:61], v[26:29], v[54:57]
	v_med3_f32 v40, v40, s50, v140
	v_mov_b32_e32 v39, 0
	v_cvt_pk_fp8_f32 v39, v117, v40
	ds_read_b128 v[54:57], v125 offset:60288
	s_waitcnt lgkmcnt(2)
	v_mfma_f32_16x16x32_bf16 v[50:53], v[70:73], v[30:33], v[50:53]
	ds_read_b128 v[70:73], v125 offset:60304
	v_lshlrev_b32_e32 v74, 16, v27
	v_and_b32_e32 v115, 0xffff0000, v27
	s_waitcnt lgkmcnt(2)
	v_mfma_f32_16x16x32_bf16 v[50:53], v[110:113], v[26:29], v[50:53]
	ds_read_b128 v[110:113], v125 offset:43392
	v_med3_f32 v41, v41, s50, v140
	v_med3_f32 v40, v116, s50, v140
	s_waitcnt lgkmcnt(2)
	v_mfma_f32_16x16x32_bf16 v[50:53], v[54:57], v[30:33], v[50:53]
	ds_read_b128 v[54:57], v125 offset:43408
	v_lshlrev_b32_e32 v121, 16, v28
	v_and_b32_e32 v143, 0xffff0000, v28
	s_waitcnt lgkmcnt(2)
	v_mfma_f32_16x16x32_bf16 v[50:53], v[70:73], v[26:29], v[50:53]
	ds_read_b128 v[70:73], v129 offset:25344
	v_cvt_pk_fp8_f32 v39, v41, v40 op_sel:[0,0,1]
	v_mul_f32_e32 v40, 4.0, v74
	s_waitcnt lgkmcnt(2)
	v_mfma_f32_16x16x32_bf16 v[34:37], v[110:113], v[30:33], v[34:37]
	v_mul_f32_e32 v41, 4.0, v115
	v_lshlrev_b32_e32 v62, 16, v26
	v_and_b32_e32 v64, 0xffff0000, v26
	s_waitcnt lgkmcnt(1)
	v_mfma_f32_16x16x32_bf16 v[34:37], v[54:57], v[26:29], v[34:37]
	ds_read_b128 v[54:57], v129 offset:25360
	v_mul_f32_e32 v48, v74, v74
	v_mul_f32_e32 v46, v115, v115
	s_waitcnt lgkmcnt(1)
	v_mfma_f32_16x16x32_bf16 v[30:33], v[70:73], v[30:33], v[34:37]
	v_med3_f32 v74, v40, s50, v140
	v_med3_f32 v115, v41, s50, v140
	v_mul_f32_e32 v40, 4.0, v121
	v_mul_f32_e32 v41, 4.0, v143
	v_lshlrev_b32_e32 v144, 16, v29
	v_and_b32_e32 v145, 0xffff0000, v29
	v_med3_f32 v40, v40, s50, v140
	v_med3_f32 v110, v41, s50, v140
	v_mov_b32_e32 v41, 0
	s_waitcnt lgkmcnt(0)
	v_mfma_f32_16x16x32_bf16 v[54:57], v[54:57], v[26:29], v[30:33]
	v_mul_f32_e32 v28, 4.0, v62
	v_mul_f32_e32 v29, 4.0, v64
	v_cvt_pk_fp8_f32 v41, v40, v110
	v_med3_f32 v28, v28, s50, v140
	v_med3_f32 v29, v29, s50, v140
	v_mov_b32_e32 v40, 0
	v_cvt_pk_fp8_f32 v40, v28, v29
	v_mul_f32_e32 v34, 4.0, v63
	v_mul_f32_e32 v35, 4.0, v65
	v_mul_f32_e32 v116, 4.0, v144
	v_mul_f32_e32 v117, 4.0, v145
	v_med3_f32 v34, v34, s50, v140
	v_med3_f32 v35, v35, s50, v140
	v_med3_f32 v111, v116, s50, v140
	v_cvt_pk_fp8_f32 v69, v34, v35 op_sel:[0,0,1]
	v_med3_f32 v34, v117, s50, v140
	v_pk_mul_f32 v[26:27], v[64:65], v[64:65]
	v_mul_f32_e32 v42, v121, v121
	v_mul_f32_e32 v44, v143, v143
	v_cvt_pk_fp8_f32 v41, v111, v34 op_sel:[0,0,1]
	v_pk_fma_f32 v[26:27], v[62:63], v[62:63], v[26:27]
	v_pk_add_f32 v[28:29], v[48:49], v[46:47]
	v_cvt_pk_fp8_f32 v40, v74, v115 op_sel:[0,0,1]
	v_mul_f32_e32 v118, v144, v144
	v_mul_f32_e32 v120, v145, v145
	v_pk_add_f32 v[26:27], v[26:27], v[28:29]
	v_pk_add_f32 v[28:29], v[42:43], v[44:45]
	v_mov_b32_e32 v121, v114
	v_pk_add_f32 v[26:27], v[26:27], v[28:29]
	v_pk_add_f32 v[28:29], v[118:119], v[120:121]
	s_add_u32 s8, s8, 0x200
	v_pk_add_f32 v[26:27], v[26:27], v[28:29]
	s_addc_u32 s9, s9, 0
	global_store_dwordx4 v[106:107], v[66:69], off
	global_store_dwordx4 v[106:107], v[38:41], off offset:64
	v_add_f32_e32 v111, v26, v27
	s_cmpk_lg_i32 s8, 0x1000
	v_lshl_add_u64 v[106:107], v[106:107], 0, s[46:47]
	s_cbranch_scc0 .LBB0_836
	s_branch .LBB0_834

.Lrouter_b:
	s_waitcnt vmcnt(12)
	v_and_b32_e32 v65, 0xffff0000, v71
	v_and_b32_e32 v64, 0xffff0000, v70
	v_lshlrev_b32_e32 v63, 16, v71
	v_lshlrev_b32_e32 v62, 16, v70
	v_pk_mul_f32 v[112:113], v[64:65], v[64:65]
	v_and_b32_e32 v155, 0xffff0000, v73
	v_and_b32_e32 v154, 0xffff0000, v72
	v_pk_fma_f32 v[112:113], v[62:63], v[62:63], v[112:113]
	v_lshlrev_b32_e32 v153, 16, v73
	v_lshlrev_b32_e32 v152, 16, v72
	v_pk_mul_f32 v[114:115], v[154:155], v[154:155]
	s_waitcnt lgkmcnt(0)
	s_barrier
	v_pk_fma_f32 v[114:115], v[152:153], v[152:153], v[114:115]
	v_add_f32_e32 v74, v112, v113
	ds_read_b128 v[144:147], v125 offset:26112
	ds_read_b128 v[148:151], v125 offset:26128
	v_add_f32_e32 v74, v114, v74
	v_lshlrev_b32_e32 v160, 16, v68
	v_pk_add_f32 v[112:113], v[114:115], v[74:75] op_sel_hi:[1,0]
	v_and_b32_e32 v161, 0xffff0000, v68
	v_mul_f32_e32 v74, v160, v160
	v_mul_f32_e32 v62, 4.0, v62
	v_mul_f32_e32 v64, 4.0, v64
	v_pk_fma_f32 v[116:117], v[160:161], v[160:161], v[74:75] op_sel_hi:[1,1,0]
	v_med3_f32 v74, v62, s48, v140
	v_med3_f32 v64, v64, s48, v140
	v_mov_b32_e32 v62, 0
	v_cvt_pk_fp8_f32 v62, v74, v64
	v_mul_f32_e32 v63, 4.0, v63
	v_mul_f32_e32 v65, 4.0, v65
	v_med3_f32 v63, v63, s48, v140
	v_med3_f32 v64, v65, s48, v140
	v_cvt_pk_fp8_f32 v62, v63, v64 op_sel:[0,0,1]
	v_mul_f32_e32 v63, 4.0, v152
	v_mul_f32_e32 v64, 4.0, v154
	v_mul_f32_e32 v65, 4.0, v153
	v_mul_f32_e32 v74, 4.0, v155
	ds_read_b128 v[152:155], v125 offset:51456
	s_waitcnt lgkmcnt(2)
	v_mfma_f32_16x16x32_bf16 v[58:61], v[144:147], v[70:73], v[58:61]
	ds_read_b128 v[144:147], v125 offset:51472
	v_med3_f32 v110, v63, s48, v140
	v_med3_f32 v64, v64, s48, v140
	s_waitcnt lgkmcnt(2)
	v_mfma_f32_16x16x32_bf16 v[58:61], v[148:151], v[66:69], v[58:61]
	ds_read_b128 v[148:151], v125 offset:34560
	v_mov_b32_e32 v63, 0
	v_cvt_pk_fp8_f32 v63, v110, v64
	s_waitcnt lgkmcnt(2)
	v_mfma_f32_16x16x32_bf16 v[58:61], v[152:155], v[70:73], v[58:61]
	ds_read_b128 v[152:155], v125 offset:34576
	v_lshlrev_b32_e32 v156, 16, v66
	v_and_b32_e32 v158, 0xffff0000, v66
	s_waitcnt lgkmcnt(2)
	v_mfma_f32_16x16x32_bf16 v[58:61], v[144:147], v[66:69], v[58:61]
	ds_read_b128 v[144:147], v125 offset:59904
	v_med3_f32 v65, v65, s48, v140
	v_med3_f32 v64, v74, s48, v140
	s_waitcnt lgkmcnt(2)
	v_mfma_f32_16x16x32_bf16 v[50:53], v[148:151], v[70:73], v[50:53]
	ds_read_b128 v[148:151], v125 offset:59920
	v_cvt_pk_fp8_f32 v63, v65, v64 op_sel:[0,0,1]
	v_mul_f32_e32 v64, 4.0, v156
	s_waitcnt lgkmcnt(2)
	v_mfma_f32_16x16x32_bf16 v[50:53], v[152:155], v[66:69], v[50:53]
	ds_read_b128 v[152:155], v125 offset:43008
	v_mul_f32_e32 v65, 4.0, v158
	v_med3_f32 v112, v64, s48, v140
	s_waitcnt lgkmcnt(2)
	v_mfma_f32_16x16x32_bf16 v[50:53], v[144:147], v[70:73], v[50:53]
	ds_read_b128 v[144:147], v125 offset:43024
	v_med3_f32 v65, v65, s48, v140
	v_mov_b32_e32 v64, 0
	s_waitcnt lgkmcnt(2)
	v_mfma_f32_16x16x32_bf16 v[50:53], v[148:151], v[66:69], v[50:53]
	ds_read_b128 v[148:151], v126 offset:25344
	v_cvt_pk_fp8_f32 v64, v112, v65
	v_lshlrev_b32_e32 v157, 16, v67
	s_waitcnt lgkmcnt(2)
	v_mfma_f32_16x16x32_bf16 v[54:57], v[152:155], v[70:73], v[54:57]
	ds_read_b128 v[152:155], v126 offset:25360
	v_and_b32_e32 v159, 0xffff0000, v67
	v_mul_f32_e32 v74, 4.0, v157
	s_waitcnt lgkmcnt(2)
	v_mfma_f32_16x16x32_bf16 v[54:57], v[144:147], v[66:69], v[54:57]
	v_mul_f32_e32 v110, 4.0, v159
	v_med3_f32 v74, v74, s48, v140
	v_med3_f32 v65, v110, s48, v140
	s_waitcnt lgkmcnt(1)
	v_mfma_f32_16x16x32_bf16 v[54:57], v[148:151], v[70:73], v[54:57]
	v_cvt_pk_fp8_f32 v64, v74, v65 op_sel:[0,0,1]
	v_mul_f32_e32 v65, 4.0, v160
	v_mul_f32_e32 v74, 4.0, v161
	v_med3_f32 v110, v65, s48, v140
	v_med3_f32 v70, v74, s48, v140
	v_mov_b32_e32 v65, 0
	s_waitcnt lgkmcnt(0)
	v_mfma_f32_16x16x32_bf16 v[54:57], v[152:155], v[66:69], v[54:57]
	s_waitcnt vmcnt(10)
	v_and_b32_e32 v149, 0xffff0000, v46
	v_and_b32_e32 v148, 0xffff0000, v48
	v_and_b32_e32 v67, 0xffff0000, v47
	v_cvt_pk_fp8_f32 v65, v110, v70
	v_lshlrev_b32_e32 v73, 16, v46
	v_lshlrev_b32_e32 v72, 16, v48
	v_lshlrev_b32_e32 v66, 16, v47
	v_mul_f32_e32 v68, v67, v67
	v_pk_mul_f32 v[70:71], v[148:149], v[148:149]
	v_lshlrev_b32_e32 v119, 16, v69
	v_and_b32_e32 v121, 0xffff0000, v69
	v_pk_fma_f32 v[68:69], v[66:67], v[66:67], v[68:69] op_sel_hi:[1,1,0]
	v_pk_fma_f32 v[70:71], v[72:73], v[72:73], v[70:71]
	v_lshlrev_b32_e32 v154, 16, v49
	v_pk_add_f32 v[68:69], v[70:71], v[68:69] op_sel:[1,0] op_sel_hi:[0,1]
	v_pk_mul_f32 v[114:115], v[158:159], v[158:159]
	v_pk_add_f32 v[152:153], v[70:71], v[68:69]
	v_and_b32_e32 v155, 0xffff0000, v49
	v_mul_f32_e32 v68, v154, v154
	v_pk_fma_f32 v[114:115], v[156:157], v[156:157], v[114:115]
	v_pk_fma_f32 v[156:157], v[154:155], v[154:155], v[68:69] op_sel_hi:[1,1,0]
	v_mul_f32_e32 v68, 4.0, v73
	v_mul_f32_e32 v69, 4.0, v149
	v_mul_f32_e32 v73, 4.0, v66
	v_med3_f32 v68, v68, s48, v140
	v_med3_f32 v69, v69, s48, v140
	v_mov_b32_e32 v66, 0
	v_cvt_pk_fp8_f32 v66, v68, v69
	ds_read_b128 v[68:71], v125 offset:26240
	ds_read_b128 v[144:147], v125 offset:26256
	v_mul_f32_e32 v67, 4.0, v67
	v_med3_f32 v73, v73, s48, v140
	v_med3_f32 v67, v67, s48, v140
	v_cvt_pk_fp8_f32 v66, v73, v67 op_sel:[0,0,1]
	v_mul_f32_e32 v67, 4.0, v72
	v_mul_f32_e32 v72, 4.0, v148
	ds_read_b128 v[148:151], v125 offset:51584
	s_waitcnt lgkmcnt(2)
	v_mfma_f32_16x16x32_bf16 v[58:61], v[68:71], v[46:49], v[58:61]
	ds_read_b128 v[68:71], v125 offset:51600
	v_mul_f32_e32 v73, 4.0, v154
	v_mul_f32_e32 v154, 4.0, v155
	s_waitcnt lgkmcnt(2)
	v_mfma_f32_16x16x32_bf16 v[58:61], v[144:147], v[42:45], v[58:61]
	ds_read_b128 v[144:147], v125 offset:34688
	v_med3_f32 v155, v67, s48, v140
	v_med3_f32 v72, v72, s48, v140
	s_waitcnt lgkmcnt(2)
	v_mfma_f32_16x16x32_bf16 v[58:61], v[148:151], v[46:49], v[58:61]
	v_mov_b32_e32 v67, 0
	v_cvt_pk_fp8_f32 v67, v155, v72
	ds_read_b128 v[148:151], v125 offset:34704
	v_med3_f32 v73, v73, s48, v140
	s_waitcnt lgkmcnt(2)
	v_mfma_f32_16x16x32_bf16 v[58:61], v[68:71], v[42:45], v[58:61]
	v_med3_f32 v68, v154, s48, v140
	v_cvt_pk_fp8_f32 v67, v73, v68 op_sel:[0,0,1]
	ds_read_b128 v[68:71], v125 offset:60032
	s_waitcnt lgkmcnt(2)
	v_mfma_f32_16x16x32_bf16 v[50:53], v[144:147], v[46:49], v[50:53]
	ds_read_b128 v[144:147], v125 offset:60048
	v_lshlrev_b32_e32 v74, 16, v43
	v_and_b32_e32 v143, 0xffff0000, v43
	s_waitcnt lgkmcnt(2)
	v_mfma_f32_16x16x32_bf16 v[50:53], v[148:151], v[42:45], v[50:53]
	ds_read_b128 v[148:151], v125 offset:43136
	v_pk_add_f32 v[114:115], v[114:115], v[114:115] op_sel_hi:[0,1]
	v_lshlrev_b32_e32 v153, 16, v44
	s_waitcnt lgkmcnt(2)
	v_mfma_f32_16x16x32_bf16 v[50:53], v[68:71], v[46:49], v[50:53]
	ds_read_b128 v[68:71], v125 offset:43152
	v_and_b32_e32 v159, 0xffff0000, v44
	v_mul_f32_e32 v72, 4.0, v74
	s_waitcnt lgkmcnt(1)
	v_mfma_f32_16x16x32_bf16 v[54:57], v[148:151], v[46:49], v[54:57]
	v_mul_f32_e32 v73, 4.0, v143
	v_mul_f32_e32 v116, v74, v74
	v_mul_f32_e32 v114, v143, v143
	v_mfma_f32_16x16x32_bf16 v[50:53], v[144:147], v[42:45], v[50:53]
	ds_read_b128 v[144:147], v127 offset:25344
	v_med3_f32 v74, v72, s48, v140
	v_med3_f32 v143, v73, s48, v140
	v_mul_f32_e32 v72, 4.0, v153
	v_mul_f32_e32 v73, 4.0, v159
	v_med3_f32 v72, v72, s48, v140
	v_med3_f32 v73, v73, s48, v140
	s_waitcnt lgkmcnt(1)
	v_mfma_f32_16x16x32_bf16 v[54:57], v[68:71], v[42:45], v[54:57]
	v_mov_b32_e32 v69, 0
	v_cvt_pk_fp8_f32 v69, v72, v73
	ds_read_b128 v[70:73], v127 offset:25360
	s_waitcnt lgkmcnt(1)
	v_mfma_f32_16x16x32_bf16 v[46:49], v[144:147], v[46:49], v[54:57]
	v_lshlrev_b32_e32 v160, 16, v45
	v_and_b32_e32 v161, 0xffff0000, v45
	v_mul_f32_e32 v110, v153, v153
	v_mul_f32_e32 v54, 4.0, v119
	v_mul_f32_e32 v55, 4.0, v121
	v_mul_f32_e32 v153, 4.0, v160
	v_mul_f32_e32 v154, 4.0, v161
	v_med3_f32 v54, v54, s48, v140
	v_med3_f32 v55, v55, s48, v140
	v_lshlrev_b32_e32 v118, 16, v42
	v_and_b32_e32 v120, 0xffff0000, v42
	v_med3_f32 v148, v153, s48, v140
	v_cvt_pk_fp8_f32 v65, v54, v55 op_sel:[0,0,1]
	v_med3_f32 v54, v154, s48, v140
	v_cvt_pk_fp8_f32 v69, v148, v54 op_sel:[0,0,1]
	s_waitcnt lgkmcnt(0)
	v_mfma_f32_16x16x32_bf16 v[54:57], v[70:73], v[42:45], v[46:49]
	v_mul_f32_e32 v44, 4.0, v118
	v_mul_f32_e32 v45, 4.0, v120
	v_med3_f32 v44, v44, s48, v140
	v_med3_f32 v45, v45, s48, v140
	v_mov_b32_e32 v68, 0
	v_cvt_pk_fp8_f32 v68, v44, v45
	v_pk_mul_f32 v[42:43], v[120:121], v[120:121]
	v_mul_f32_e32 v112, v159, v159
	v_pk_fma_f32 v[42:43], v[118:119], v[118:119], v[42:43]
	v_cvt_pk_fp8_f32 v68, v74, v143 op_sel:[0,0,1]
	v_pk_add_f32 v[44:45], v[116:117], v[114:115]
	v_mul_f32_e32 v156, v160, v160
	v_mul_f32_e32 v158, v161, v161
	v_pk_add_f32 v[42:43], v[42:43], v[44:45]
	v_pk_add_f32 v[44:45], v[110:111], v[112:113]
	v_mov_b32_e32 v159, v152
	v_pk_add_f32 v[42:43], v[42:43], v[44:45]
	v_pk_add_f32 v[44:45], v[156:157], v[158:159]
	global_store_dwordx4 v[106:107], v[66:69], off offset:-64
	v_pk_add_f32 v[42:43], v[42:43], v[44:45]
	s_waitcnt vmcnt(9)
	v_and_b32_e32 v115, 0xffff0000, v41
	v_and_b32_e32 v69, 0xffff0000, v39
	v_and_b32_e32 v68, 0xffff0000, v38
	v_lshlrev_b32_e32 v67, 16, v39
	v_lshlrev_b32_e32 v66, 16, v38
	v_pk_mul_f32 v[44:45], v[68:69], v[68:69]
	v_and_b32_e32 v114, 0xffff0000, v40
	v_pk_add_f32 v[42:43], v[42:43], v[42:43] op_sel_hi:[0,1]
	v_pk_fma_f32 v[44:45], v[66:67], v[66:67], v[44:45]
	v_lshlrev_b32_e32 v73, 16, v41
	v_lshlrev_b32_e32 v72, 16, v40
	v_pk_mul_f32 v[46:47], v[114:115], v[114:115]
	v_add_f32_e32 v42, v44, v45
	v_pk_fma_f32 v[46:47], v[72:73], v[72:73], v[46:47]
	v_lshlrev_b32_e32 v144, 16, v36
	v_add_f32_e32 v42, v46, v42
	v_pk_add_f32 v[44:45], v[46:47], v[42:43] op_sel_hi:[1,0]
	v_and_b32_e32 v145, 0xffff0000, v36
	v_mul_f32_e32 v42, v144, v144
	v_pk_fma_f32 v[48:49], v[144:145], v[144:145], v[42:43] op_sel_hi:[1,1,0]
	v_mul_f32_e32 v44, 4.0, v68
	v_mul_f32_e32 v48, 4.0, v69
	ds_read_b128 v[68:71], v125 offset:26368
	ds_read_b128 v[110:113], v125 offset:26384
	v_and_b32_e32 v121, 0xffff0000, v35
	v_and_b32_e32 v120, 0xffff0000, v34
	v_mul_f32_e32 v42, 4.0, v66
	v_lshlrev_b32_e32 v119, 16, v35
	v_lshlrev_b32_e32 v118, 16, v34
	v_pk_mul_f32 v[46:47], v[120:121], v[120:121]
	v_med3_f32 v42, v42, s48, v140
	v_med3_f32 v44, v44, s48, v140
	v_mov_b32_e32 v66, 0
	v_pk_fma_f32 v[46:47], v[118:119], v[118:119], v[46:47]
	v_cvt_pk_fp8_f32 v66, v42, v44
	v_pk_add_f32 v[46:47], v[46:47], v[46:47] op_sel_hi:[0,1]
	v_mul_f32_e32 v46, 4.0, v67
	v_med3_f32 v42, v46, s48, v140
	v_med3_f32 v44, v48, s48, v140
	v_cvt_pk_fp8_f32 v66, v42, v44 op_sel:[0,0,1]
	v_mul_f32_e32 v44, 4.0, v114
	v_mul_f32_e32 v48, 4.0, v115
	ds_read_b128 v[114:117], v125 offset:51712
	s_waitcnt lgkmcnt(2)
	v_mfma_f32_16x16x32_bf16 v[58:61], v[68:71], v[38:41], v[58:61]
	ds_read_b128 v[68:71], v125 offset:51728
	v_mul_f32_e32 v42, 4.0, v72
	v_mul_f32_e32 v46, 4.0, v73
	s_waitcnt lgkmcnt(2)
	v_mfma_f32_16x16x32_bf16 v[58:61], v[110:113], v[34:37], v[58:61]
	ds_read_b128 v[110:113], v125 offset:34816
	v_med3_f32 v42, v42, s48, v140
	v_med3_f32 v44, v44, s48, v140
	s_waitcnt lgkmcnt(2)
	v_mfma_f32_16x16x32_bf16 v[58:61], v[114:117], v[38:41], v[58:61]
	ds_read_b128 v[114:117], v125 offset:34832
	v_mov_b32_e32 v67, 0
	v_cvt_pk_fp8_f32 v67, v42, v44
	s_waitcnt lgkmcnt(2)
	v_mfma_f32_16x16x32_bf16 v[58:61], v[68:71], v[34:37], v[58:61]
	ds_read_b128 v[68:71], v125 offset:60160
	v_med3_f32 v46, v46, s48, v140
	v_med3_f32 v42, v48, s48, v140
	s_waitcnt lgkmcnt(2)
	v_mfma_f32_16x16x32_bf16 v[50:53], v[110:113], v[38:41], v[50:53]
	ds_read_b128 v[110:113], v125 offset:60176
	v_cvt_pk_fp8_f32 v67, v46, v42 op_sel:[0,0,1]
	v_mul_f32_e32 v42, 4.0, v118
	s_waitcnt lgkmcnt(2)
	v_mfma_f32_16x16x32_bf16 v[50:53], v[114:117], v[34:37], v[50:53]
	ds_read_b128 v[114:117], v125 offset:43264
	v_mul_f32_e32 v44, 4.0, v120
	v_med3_f32 v42, v42, s48, v140
	s_waitcnt lgkmcnt(2)
	v_mfma_f32_16x16x32_bf16 v[50:53], v[68:71], v[38:41], v[50:53]
	ds_read_b128 v[70:73], v125 offset:43280
	v_med3_f32 v44, v44, s48, v140
	v_mov_b32_e32 v68, 0
	s_waitcnt lgkmcnt(2)
	v_mfma_f32_16x16x32_bf16 v[50:53], v[110:113], v[34:37], v[50:53]
	ds_read_b128 v[110:113], v128 offset:25344
	v_cvt_pk_fp8_f32 v68, v42, v44
	v_mul_f32_e32 v46, 4.0, v119
	s_waitcnt lgkmcnt(2)
	v_mfma_f32_16x16x32_bf16 v[54:57], v[114:117], v[38:41], v[54:57]
	ds_read_b128 v[114:117], v128 offset:25360
	v_mul_f32_e32 v48, 4.0, v121
	v_med3_f32 v46, v46, s48, v140
	s_waitcnt lgkmcnt(2)
	v_mfma_f32_16x16x32_bf16 v[54:57], v[70:73], v[34:37], v[54:57]
	v_med3_f32 v42, v48, s48, v140
	v_cvt_pk_fp8_f32 v68, v46, v42 op_sel:[0,0,1]
	v_mul_f32_e32 v42, 4.0, v144
	s_waitcnt lgkmcnt(1)
	v_mfma_f32_16x16x32_bf16 v[38:41], v[110:113], v[38:41], v[54:57]
	v_mul_f32_e32 v44, 4.0, v145
	global_store_dwordx4 v[106:107], v[62:65], off offset:-128
	v_med3_f32 v42, v42, s48, v140
	v_med3_f32 v44, v44, s48, v140
	v_lshlrev_b32_e32 v63, 16, v37
	v_and_b32_e32 v65, 0xffff0000, v37
	v_mov_b32_e32 v69, 0
	s_waitcnt lgkmcnt(0)
	v_mfma_f32_16x16x32_bf16 v[34:37], v[114:117], v[34:37], v[38:41]
	s_waitcnt vmcnt(8)
	v_and_b32_e32 v111, 0xffff0000, v30
	v_and_b32_e32 v110, 0xffff0000, v32
	v_cvt_pk_fp8_f32 v69, v42, v44
	v_and_b32_e32 v39, 0xffff0000, v31
	v_lshlrev_b32_e32 v41, 16, v30
	v_lshlrev_b32_e32 v40, 16, v32
	v_lshlrev_b32_e32 v38, 16, v31
	v_mul_f32_e32 v42, v39, v39
	v_pk_mul_f32 v[56:57], v[110:111], v[110:111]
	v_pk_fma_f32 v[54:55], v[38:39], v[38:39], v[42:43] op_sel_hi:[1,1,0]
	v_pk_fma_f32 v[56:57], v[40:41], v[40:41], v[56:57]
	v_mul_f32_e32 v41, 4.0, v41
	v_pk_add_f32 v[54:55], v[56:57], v[54:55] op_sel:[1,0] op_sel_hi:[0,1]
	v_pk_add_f32 v[114:115], v[56:57], v[54:55]
	v_mul_f32_e32 v54, 4.0, v111
	v_mul_f32_e32 v70, 4.0, v38
	v_med3_f32 v41, v41, s48, v140
	v_med3_f32 v54, v54, s48, v140
	v_mov_b32_e32 v38, 0
	v_cvt_pk_fp8_f32 v38, v41, v54
	ds_read_b128 v[54:57], v125 offset:26496
	v_med3_f32 v41, v70, s48, v140
	ds_read_b128 v[70:73], v125 offset:26512
	v_mul_f32_e32 v39, 4.0, v39
	v_med3_f32 v39, v39, s48, v140
	v_cvt_pk_fp8_f32 v38, v41, v39 op_sel:[0,0,1]
	v_mul_f32_e32 v39, 4.0, v40
	v_mul_f32_e32 v40, 4.0, v110
	ds_read_b128 v[110:113], v125 offset:51840
	s_waitcnt lgkmcnt(2)
	v_mfma_f32_16x16x32_bf16 v[54:57], v[54:57], v[30:33], v[58:61]
	v_lshlrev_b32_e32 v116, 16, v33
	v_and_b32_e32 v117, 0xffff0000, v33
	v_mul_f32_e32 v42, v116, v116
	ds_read_b128 v[58:61], v125 offset:51856
	s_waitcnt lgkmcnt(2)
	v_mfma_f32_16x16x32_bf16 v[54:57], v[70:73], v[26:29], v[54:57]
	ds_read_b128 v[70:73], v125 offset:34944
	v_pk_fma_f32 v[118:119], v[116:117], v[116:117], v[42:43] op_sel_hi:[1,1,0]
	v_mul_f32_e32 v41, 4.0, v116
	s_waitcnt lgkmcnt(2)
	v_mfma_f32_16x16x32_bf16 v[54:57], v[110:113], v[30:33], v[54:57]
	ds_read_b128 v[110:113], v125 offset:34960
	v_mul_f32_e32 v116, 4.0, v117
	v_med3_f32 v117, v39, s48, v140
	s_waitcnt lgkmcnt(2)
	v_mfma_f32_16x16x32_bf16 v[58:61], v[58:61], v[26:29], v[54:57]
	v_med3_f32 v40, v40, s48, v140
	v_mov_b32_e32 v39, 0
	v_cvt_pk_fp8_f32 v39, v117, v40
	ds_read_b128 v[54:57], v125 offset:60288
	s_waitcnt lgkmcnt(2)
	v_mfma_f32_16x16x32_bf16 v[50:53], v[70:73], v[30:33], v[50:53]
	ds_read_b128 v[70:73], v125 offset:60304
	v_lshlrev_b32_e32 v74, 16, v27
	v_and_b32_e32 v115, 0xffff0000, v27
	s_waitcnt lgkmcnt(2)
	v_mfma_f32_16x16x32_bf16 v[50:53], v[110:113], v[26:29], v[50:53]
	ds_read_b128 v[110:113], v125 offset:43392
	v_med3_f32 v41, v41, s48, v140
	v_med3_f32 v40, v116, s48, v140
	s_waitcnt lgkmcnt(2)
	v_mfma_f32_16x16x32_bf16 v[50:53], v[54:57], v[30:33], v[50:53]
	ds_read_b128 v[54:57], v125 offset:43408
	v_lshlrev_b32_e32 v121, 16, v28
	v_and_b32_e32 v143, 0xffff0000, v28
	s_waitcnt lgkmcnt(2)
	v_mfma_f32_16x16x32_bf16 v[50:53], v[70:73], v[26:29], v[50:53]
	ds_read_b128 v[70:73], v129 offset:25344
	v_cvt_pk_fp8_f32 v39, v41, v40 op_sel:[0,0,1]
	v_mul_f32_e32 v40, 4.0, v74
	s_waitcnt lgkmcnt(2)
	v_mfma_f32_16x16x32_bf16 v[34:37], v[110:113], v[30:33], v[34:37]
	v_mul_f32_e32 v41, 4.0, v115
	v_lshlrev_b32_e32 v62, 16, v26
	v_and_b32_e32 v64, 0xffff0000, v26
	s_waitcnt lgkmcnt(1)
	v_mfma_f32_16x16x32_bf16 v[34:37], v[54:57], v[26:29], v[34:37]
	ds_read_b128 v[54:57], v129 offset:25360
	v_mul_f32_e32 v48, v74, v74
	v_mul_f32_e32 v46, v115, v115
	s_waitcnt lgkmcnt(1)
	v_mfma_f32_16x16x32_bf16 v[30:33], v[70:73], v[30:33], v[34:37]
	v_med3_f32 v74, v40, s48, v140
	v_med3_f32 v115, v41, s48, v140
	v_mul_f32_e32 v40, 4.0, v121
	v_mul_f32_e32 v41, 4.0, v143
	v_lshlrev_b32_e32 v144, 16, v29
	v_and_b32_e32 v145, 0xffff0000, v29
	v_med3_f32 v40, v40, s48, v140
	v_med3_f32 v110, v41, s48, v140
	v_mov_b32_e32 v41, 0
	s_waitcnt lgkmcnt(0)
	v_mfma_f32_16x16x32_bf16 v[54:57], v[54:57], v[26:29], v[30:33]
	v_mul_f32_e32 v28, 4.0, v62
	v_mul_f32_e32 v29, 4.0, v64
	v_cvt_pk_fp8_f32 v41, v40, v110
	v_med3_f32 v28, v28, s48, v140
	v_med3_f32 v29, v29, s48, v140
	v_mov_b32_e32 v40, 0
	v_cvt_pk_fp8_f32 v40, v28, v29
	v_mul_f32_e32 v34, 4.0, v63
	v_mul_f32_e32 v35, 4.0, v65
	v_mul_f32_e32 v116, 4.0, v144
	v_mul_f32_e32 v117, 4.0, v145
	v_med3_f32 v34, v34, s48, v140
	v_med3_f32 v35, v35, s48, v140
	v_med3_f32 v111, v116, s48, v140
	v_cvt_pk_fp8_f32 v69, v34, v35 op_sel:[0,0,1]
	v_med3_f32 v34, v117, s48, v140
	v_pk_mul_f32 v[26:27], v[64:65], v[64:65]
	v_mul_f32_e32 v42, v121, v121
	v_mul_f32_e32 v44, v143, v143
	v_cvt_pk_fp8_f32 v41, v111, v34 op_sel:[0,0,1]
	v_pk_fma_f32 v[26:27], v[62:63], v[62:63], v[26:27]
	v_pk_add_f32 v[28:29], v[48:49], v[46:47]
	v_cvt_pk_fp8_f32 v40, v74, v115 op_sel:[0,0,1]
	v_mul_f32_e32 v118, v144, v144
	v_mul_f32_e32 v120, v145, v145
	v_pk_add_f32 v[26:27], v[26:27], v[28:29]
	v_pk_add_f32 v[28:29], v[42:43], v[44:45]
	v_mov_b32_e32 v121, v114
	v_pk_add_f32 v[26:27], v[26:27], v[28:29]
	v_pk_add_f32 v[28:29], v[118:119], v[120:121]
	s_add_u32 s6, s6, 0x200
	v_pk_add_f32 v[26:27], v[26:27], v[28:29]
	s_addc_u32 s7, s7, 0
	global_store_dwordx4 v[106:107], v[66:69], off
	global_store_dwordx4 v[106:107], v[38:41], off offset:64
	v_add_f32_e32 v111, v26, v27
	s_cmpk_lg_i32 s6, 0x1000
	v_lshl_add_u64 v[106:107], v[106:107], 0, s[44:45]
	s_cbranch_scc0 .LBB0_1447
	s_branch .LBB0_1445
